# speedup vs baseline: 1.0517x; 1.0517x over previous
.LBB0_7:
	s_or_b64 exec, exec, s[0:1]
	s_waitcnt lgkmcnt(0)
	s_barrier
	ds_read_b128 v[0:3], v30
	s_add_u32 s0, s6, s4
	s_addc_u32 s1, s7, s5
	v_add_u32_e32 v14, v15, v14
	ds_read_b128 v[4:7], v14 offset:16384
	s_waitcnt lgkmcnt(1)
	global_store_dwordx4 v30, v[0:3], s[0:1] sc0 sc1
	ds_read_b128 v[0:3], v14 offset:4096
	v_lshl_add_u64 v[16:17], s[0:1], 0, v[30:31]
	v_add_co_u32_e32 v12, vcc, 0x1000, v16
	ds_read_b128 v[8:11], v49
	s_nop 0
	v_addc_co_u32_e32 v13, vcc, 0, v17, vcc
	s_waitcnt lgkmcnt(1)
	global_store_dwordx4 v[12:13], v[0:3], off sc0 sc1
	ds_read_b128 v[0:3], v14 offset:8192
	ds_read_b128 v[12:15], v14 offset:12288
	v_add_co_u32_e32 v18, vcc, 0x2000, v16
	s_nop 1
	v_addc_co_u32_e32 v19, vcc, 0, v17, vcc
	s_waitcnt lgkmcnt(1)
	global_store_dwordx4 v[18:19], v[0:3], off sc0 sc1
	s_nop 1
	v_add_co_u32_e32 v0, vcc, 0x3000, v16
	s_nop 1
	v_addc_co_u32_e32 v1, vcc, 0, v17, vcc
	s_waitcnt lgkmcnt(0)
	global_store_dwordx4 v[0:1], v[12:15], off sc0 sc1
	v_lshlrev_b32_e32 v0, 4, v48
	global_store_dwordx4 v0, v[4:7], s[0:1] sc0 sc1
	global_store_dwordx4 v49, v[8:11], s[0:1] sc0 sc1
	s_endpgm
